# baseline (speedup 1.0000x reference)
.LBB1_2:
	s_or_b64 exec, exec, s[8:9]
	s_ashr_i32 s9, s2, 3
	s_and_b32 s8, s2, 7
	s_and_b32 s9, s9, -8
	s_bfe_u32 s20, s3, 0x20006
	s_or_b32 s10, s9, s8
	s_lshl_b32 s2, s2, 4
	s_lshr_b32 s22, s3, 6
	v_bfe_u32 v1, v0, 5, 1
	s_and_b32 s2, s2, 0x380
	s_lshl_b32 s8, s20, 5
	s_ashr_i32 s11, s10, 31
	s_or_b32 s2, s8, s2
	s_lshl_b64 s[8:9], s[10:11], 19
	v_lshl_or_b32 v2, s22, 1, v1
	s_waitcnt lgkmcnt(0)
	s_cmpk_gt_u32 s3, 0xff
	s_cselect_b32 s44, s46, s44
	s_cselect_b32 s45, s47, s45
	v_and_b32_e32 v108, 0xff, v0
	v_lshlrev_b32_e32 v108, 2, v108
	global_load_dword v108, v108, s[44:45]
	s_add_u32 s14, s4, s8
	v_lshlrev_b32_e32 v6, 9, v2
	v_lshlrev_b32_e32 v2, 2, v2
	v_and_b32_e32 v5, 31, v0
	s_addc_u32 s15, s5, s9
	v_and_b32_e32 v2, 12, v2
	s_bfe_u32 s4, s3, 0x20007
	v_bitop3_b32 v2, v2, v5, s4 bitop3:0x36
	s_lshl_b32 s4, s22, 10
	v_lshl_or_b32 v192, v2, 4, v6
	s_add_i32 s21, s4, 0
	s_mov_b32 s4, m0
	s_mov_b32 m0, s21
	s_nop 0
	global_load_lds_dwordx4 v192, s[6:7]
	s_mov_b32 m0, s4
	s_add_u32 s4, s6, 0x2000
	s_addc_u32 s5, s7, 0
	s_add_i32 s31, s21, 0x2000
	s_mov_b32 s8, m0
	s_mov_b32 m0, s31
	s_nop 0
	global_load_lds_dwordx4 v192, s[4:5]
	s_mov_b32 m0, s8
	s_add_u32 s4, s6, 0x4000
	s_addc_u32 s5, s7, 0
	s_add_i32 s33, s21, 0x4000
	s_mov_b32 s8, m0
	s_mov_b32 m0, s33
	s_nop 0
	global_load_lds_dwordx4 v192, s[4:5]
	s_mov_b32 m0, s8
	s_add_u32 s4, s6, 0x6000
	s_addc_u32 s5, s7, 0
	s_add_i32 s34, s21, 0x6000
	s_mov_b32 s8, m0
	s_mov_b32 m0, s34
	s_nop 0
	global_load_lds_dwordx4 v192, s[4:5]
	s_mov_b32 m0, s8
	s_add_u32 s4, s6, 0x8000
	s_addc_u32 s5, s7, 0
	s_add_i32 s23, s21, 0x8000
	s_mov_b32 s8, m0
	s_mov_b32 m0, s23
	s_nop 0
	global_load_lds_dwordx4 v192, s[4:5]
	s_mov_b32 m0, s8
	s_add_u32 s4, s6, 0xa000
	s_addc_u32 s5, s7, 0
	s_add_i32 s24, s21, 0xa000
	s_mov_b32 s8, m0
	s_mov_b32 m0, s24
	s_nop 0
	global_load_lds_dwordx4 v192, s[4:5]
	s_mov_b32 m0, s8
	s_add_u32 s4, s6, 0xc000
	s_addc_u32 s5, s7, 0
	s_add_i32 s25, s21, 0xc000
	s_mov_b32 s8, m0
	s_mov_b32 m0, s25
	s_nop 0
	global_load_lds_dwordx4 v192, s[4:5]
	s_mov_b32 m0, s8
	s_add_u32 s4, s6, 0xe000
	s_addc_u32 s5, s7, 0
	s_add_i32 s26, s21, 0xe000
	s_mov_b32 s8, m0
	s_mov_b32 m0, s26
	s_nop 0
	global_load_lds_dwordx4 v192, s[4:5]
	s_mov_b32 m0, s8
	s_and_b32 s4, s2, 0x380
	s_lshl_b32 s4, s4, 9
	s_add_u32 s4, s14, s4
	s_addc_u32 s5, s15, 0
	s_add_i32 s27, s21, 0x10000
	s_add_i32 s28, s21, 0x12000
	s_add_i32 s29, s21, 0x14000
	s_add_i32 s30, s21, 0x16000
	s_mov_b32 s8, m0
	s_mov_b32 m0, s27
	s_nop 0
	global_load_lds_dwordx4 v192, s[4:5]
	s_mov_b32 m0, s8
	s_add_u32 s40, s4, 0x2000
	s_addc_u32 s41, s5, 0
	s_mov_b32 s8, m0
	s_mov_b32 m0, s28
	s_nop 0
	global_load_lds_dwordx4 v192, s[40:41]
	s_mov_b32 m0, s8
	s_add_u32 s40, s4, 0x4000
	s_addc_u32 s41, s5, 0
	s_mov_b32 s8, m0
	s_mov_b32 m0, s29
	s_nop 0
	global_load_lds_dwordx4 v192, s[40:41]
	s_mov_b32 m0, s8
	s_add_u32 s40, s4, 0x6000
	s_addc_u32 s41, s5, 0
	s_mov_b32 s8, m0
	s_mov_b32 m0, s30
	s_nop 0
	global_load_lds_dwordx4 v192, s[40:41]
	s_mov_b32 m0, s8
	s_add_u32 s40, s4, 0x8000
	s_addc_u32 s41, s5, 0
	s_add_i32 s42, s21, 0x18000
	s_mov_b32 s8, m0
	s_mov_b32 m0, s42
	s_nop 0
	global_load_lds_dwordx4 v192, s[40:41]
	s_mov_b32 m0, s8
	s_add_u32 s40, s4, 0xa000
	s_addc_u32 s41, s5, 0
	s_add_i32 s42, s21, 0x1a000
	s_mov_b32 s8, m0
	s_mov_b32 m0, s42
	s_nop 0
	global_load_lds_dwordx4 v192, s[40:41]
	s_mov_b32 m0, s8
	s_add_u32 s40, s4, 0xc000
	s_addc_u32 s41, s5, 0
	s_add_i32 s42, s21, 0x1c000
	s_mov_b32 s8, m0
	s_mov_b32 m0, s42
	s_nop 0
	global_load_lds_dwordx4 v192, s[40:41]
	s_mov_b32 m0, s8
	s_add_u32 s40, s4, 0xe000
	s_addc_u32 s41, s5, 0
	s_add_i32 s42, s21, 0x1e000
	s_mov_b32 s8, m0
	s_mov_b32 m0, s42
	s_nop 0
	global_load_lds_dwordx4 v192, s[40:41]
	s_mov_b32 m0, s8
	s_load_dwordx2 s[8:9], s[0:1], 0x18
	s_load_dwordx2 s[12:13], s[0:1], 0x28
	v_and_b32_e32 v81, 63, v0
	v_lshlrev_b32_e32 v2, 2, v0
	v_add_u32_e32 v6, 0x22000, v2
	s_waitcnt vmcnt(16)
	ds_write_b32 v6, v108
	s_lshr_b32 s5, s3, 8
	s_lshl_b32 s16, s20, 12
	s_lshl_b32 s4, s5, 5
	s_add_i32 s35, s16, 0
	s_add_u32 s18, s6, 0x18000
	v_and_b32_e32 v2, 12, v2
	v_bfe_u32 v0, v0, 2, 2
	s_addc_u32 s19, s7, 0
	v_bitop3_b32 v0, v2, v1, v0 bitop3:0x36
	s_add_u32 s16, s14, 0x8000
	v_lshlrev_b32_e32 v100, 4, v0
	v_or_b32_e32 v0, s4, v5
	s_addc_u32 s17, s15, 0
	s_lshl_b32 s36, s5, 7
	v_lshl_add_u32 v101, v0, 9, 0
	v_lshl_or_b32 v0, v1, 4, s36
	v_add_u32_e32 v0, 0, v0
	v_add_u32_e32 v83, v101, v100
	s_waitcnt vmcnt(0)
	s_waitcnt lgkmcnt(0)
	s_barrier
	v_add_u32_e32 v80, 0x22000, v0
	s_lshl_b32 s40, s20, 14
	s_add_i32 s40, s40, 0x10000
	v_lshl_add_u32 v224, v5, 9, s40
	ds_read_b128 v[0:3], v80 offset:0
	ds_read_b128 v[4:7], v80 offset:32
	ds_read_b128 v[8:11], v80 offset:64
	ds_read_b128 v[12:15], v80 offset:96
	v_add_u32_e32 v225, v224, v100
	ds_read_b128 v[68:71], v225
	ds_read_b128 v[76:79], v225 offset:256
	ds_read_b128 v[92:95], v83
	ds_read_b128 v[96:99], v83 offset:256
	v_xor_b32_e32 v84, 0x20, v100
	v_add_u32_e32 v84, v101, v84
	v_xor_b32_e32 v225, 0x20, v100
	v_add_u32_e32 v225, v224, v225
	ds_read_b128 v[60:63], v225
	ds_read_b128 v[72:75], v225 offset:256
	ds_read_b128 v[200:203], v84
	ds_read_b128 v[204:207], v84 offset:256
	v_xor_b32_e32 v225, 0x40, v100
	v_add_u32_e32 v225, v224, v225
	ds_read_b128 v[52:55], v225
	ds_read_b128 v[64:67], v225 offset:256
	v_xor_b32_e32 v225, 0x60, v100
	v_add_u32_e32 v225, v224, v225
	ds_read_b128 v[48:51], v225
	ds_read_b128 v[56:59], v225 offset:256
	v_xor_b32_e32 v225, 0x80, v100
	v_add_u32_e32 v225, v224, v225
	ds_read_b128 v[36:39], v225
	ds_read_b128 v[44:47], v225 offset:256
	v_xor_b32_e32 v225, 0xa0, v100
	v_add_u32_e32 v225, v224, v225
	ds_read_b128 v[28:31], v225
	ds_read_b128 v[40:43], v225 offset:256
	v_xor_b32_e32 v225, 0xc0, v100
	v_add_u32_e32 v225, v224, v225
	ds_read_b128 v[24:27], v225
	ds_read_b128 v[32:35], v225 offset:256
	v_xor_b32_e32 v225, 0xe0, v100
	v_add_u32_e32 v225, v224, v225
	ds_read_b128 v[20:23], v225
	ds_read_b128 v[16:19], v225 offset:256
	ds_read_b128 v[108:111], v80 offset:256
	ds_read_b128 v[112:115], v80 offset:288
	ds_read_b128 v[116:119], v80 offset:320
	ds_read_b128 v[120:123], v80 offset:352
	v_lshl_add_u32 v81, v81, 4, s35
	v_add_u32_e32 v81, 0x18000, v81
	v_lshl_add_u32 v82, s5, 11, v81
	v_xor_b32_e32 v85, 0x40, v100
	v_add_u32_e32 v85, v101, v85
	v_xor_b32_e32 v86, 0x60, v100
	v_add_u32_e32 v86, v101, v86
	v_xor_b32_e32 v87, 0x80, v100
	v_add_u32_e32 v87, v101, v87
	v_xor_b32_e32 v88, 0xa0, v100
	v_add_u32_e32 v88, v101, v88
	v_xor_b32_e32 v89, 0xc0, v100
	v_add_u32_e32 v89, v101, v89
	v_xor_b32_e32 v90, 0xe0, v100
	v_add_u32_e32 v90, v101, v90
	v_add_u32_e32 v208, 0x10000, v83
	v_add_u32_e32 v209, 0x10000, v84
	v_add_u32_e32 v210, 0x10000, v85
	v_add_u32_e32 v211, 0x10000, v86
	v_add_u32_e32 v212, 0x10000, v87
	v_add_u32_e32 v213, 0x10000, v88
	v_add_u32_e32 v214, 0x10000, v89
	v_add_u32_e32 v215, 0x10000, v90
	s_waitcnt lgkmcnt(15)
	s_waitcnt lgkmcnt(15)
	s_waitcnt lgkmcnt(15)
	v_mfma_f32_32x32x16_bf16 v[0:15], v[92:95], v[68:71], v[0:15]
	s_waitcnt lgkmcnt(15)
	v_mfma_f32_32x32x16_bf16 v[0:15], v[96:99], v[76:79], v[0:15]
	ds_read_b128 v[92:95], v85
	ds_read_b128 v[96:99], v85 offset:256
	s_waitcnt lgkmcnt(15)
	s_waitcnt lgkmcnt(15)
	v_mfma_f32_32x32x16_bf16 v[0:15], v[200:203], v[60:63], v[0:15]
	s_waitcnt lgkmcnt(15)
	v_mfma_f32_32x32x16_bf16 v[0:15], v[204:207], v[72:75], v[0:15]
	ds_read_b128 v[200:203], v86
	ds_read_b128 v[204:207], v86 offset:256
	s_waitcnt lgkmcnt(15)
	s_waitcnt lgkmcnt(3)
	v_mfma_f32_32x32x16_bf16 v[0:15], v[92:95], v[52:55], v[0:15]
	s_waitcnt lgkmcnt(2)
	v_mfma_f32_32x32x16_bf16 v[0:15], v[96:99], v[64:67], v[0:15]
	ds_read_b128 v[92:95], v87
	ds_read_b128 v[96:99], v87 offset:256
	s_waitcnt lgkmcnt(10)
	s_barrier
	s_add_u32 s40, s6, 0x10000
	s_addc_u32 s41, s7, 0
	s_mov_b32 s42, m0
	s_mov_b32 m0, s27
	s_nop 0
	global_load_lds_dwordx4 v192, s[40:41]
	s_mov_b32 m0, s42
	s_add_u32 s40, s6, 0x12000
	s_addc_u32 s41, s7, 0
	s_mov_b32 s42, m0
	s_mov_b32 m0, s28
	s_nop 0
	global_load_lds_dwordx4 v192, s[40:41]
	s_mov_b32 m0, s42
	s_add_u32 s40, s6, 0x14000
	s_addc_u32 s41, s7, 0
	s_mov_b32 s42, m0
	s_mov_b32 m0, s29
	s_nop 0
	global_load_lds_dwordx4 v192, s[40:41]
	s_mov_b32 m0, s42
	s_add_u32 s40, s6, 0x16000
	s_addc_u32 s41, s7, 0
	s_mov_b32 s42, m0
	s_mov_b32 m0, s30
	s_nop 0
	global_load_lds_dwordx4 v192, s[40:41]
	s_mov_b32 m0, s42
	s_waitcnt lgkmcnt(15)
	s_waitcnt lgkmcnt(3)
	v_mfma_f32_32x32x16_bf16 v[0:15], v[200:203], v[48:51], v[0:15]
	s_waitcnt lgkmcnt(2)
	v_mfma_f32_32x32x16_bf16 v[0:15], v[204:207], v[56:59], v[0:15]
	ds_read_b128 v[200:203], v88
	ds_read_b128 v[204:207], v88 offset:256
	s_waitcnt lgkmcnt(15)
	s_waitcnt lgkmcnt(3)
	v_mfma_f32_32x32x16_bf16 v[0:15], v[92:95], v[36:39], v[0:15]
	s_waitcnt lgkmcnt(2)
	v_mfma_f32_32x32x16_bf16 v[0:15], v[96:99], v[44:47], v[0:15]
	ds_read_b128 v[92:95], v89
	ds_read_b128 v[96:99], v89 offset:256
	s_waitcnt lgkmcnt(15)
	s_waitcnt lgkmcnt(3)
	v_mfma_f32_32x32x16_bf16 v[0:15], v[200:203], v[28:31], v[0:15]
	s_waitcnt lgkmcnt(2)
	v_mfma_f32_32x32x16_bf16 v[0:15], v[204:207], v[40:43], v[0:15]
	ds_read_b128 v[200:203], v90
	ds_read_b128 v[204:207], v90 offset:256
	s_waitcnt lgkmcnt(15)
	s_waitcnt lgkmcnt(3)
	v_mfma_f32_32x32x16_bf16 v[0:15], v[92:95], v[24:27], v[0:15]
	s_waitcnt lgkmcnt(2)
	v_mfma_f32_32x32x16_bf16 v[0:15], v[96:99], v[32:35], v[0:15]
	ds_read_b128 v[92:95], v83 offset:32768
	ds_read_b128 v[96:99], v83 offset:33024
	s_waitcnt lgkmcnt(15)
	s_waitcnt lgkmcnt(3)
	v_mfma_f32_32x32x16_bf16 v[0:15], v[200:203], v[20:23], v[0:15]
	s_waitcnt lgkmcnt(2)
	v_mfma_f32_32x32x16_bf16 v[0:15], v[204:207], v[16:19], v[0:15]
	ds_read_b128 v[200:203], v84 offset:32768
	ds_read_b128 v[204:207], v84 offset:33024
	s_waitcnt lgkmcnt(15)
	s_waitcnt lgkmcnt(3)
	v_mfma_f32_32x32x16_bf16 v[108:123], v[92:95], v[68:71], v[108:123]
	s_waitcnt lgkmcnt(2)
	v_mfma_f32_32x32x16_bf16 v[108:123], v[96:99], v[76:79], v[108:123]
	ds_read_b128 v[92:95], v85 offset:32768
	ds_read_b128 v[96:99], v85 offset:33024
	s_waitcnt lgkmcnt(3)
	v_mfma_f32_32x32x16_bf16 v[108:123], v[200:203], v[60:63], v[108:123]
	s_waitcnt lgkmcnt(2)
	v_mfma_f32_32x32x16_bf16 v[108:123], v[204:207], v[72:75], v[108:123]
	ds_read_b128 v[200:203], v86 offset:32768
	ds_read_b128 v[204:207], v86 offset:33024
	s_nop 1
	v_cvt_pk_bf16_f32 v216, v0, v1
	v_cvt_pk_bf16_f32 v217, v2, v3
	v_cvt_pk_bf16_f32 v218, v4, v5
	v_cvt_pk_bf16_f32 v219, v6, v7
	s_waitcnt lgkmcnt(3)
	v_mfma_f32_32x32x16_bf16 v[108:123], v[92:95], v[52:55], v[108:123]
	s_waitcnt lgkmcnt(2)
	v_mfma_f32_32x32x16_bf16 v[108:123], v[96:99], v[64:67], v[108:123]
	ds_read_b128 v[92:95], v87 offset:32768
	ds_read_b128 v[96:99], v87 offset:33024
	v_cvt_pk_bf16_f32 v220, v8, v9
	v_cvt_pk_bf16_f32 v221, v10, v11
	v_cvt_pk_bf16_f32 v222, v12, v13
	v_cvt_pk_bf16_f32 v223, v14, v15
	ds_write_b128 v82, v[216:219]
	ds_write_b128 v82, v[220:223] offset:1024
	s_waitcnt lgkmcnt(5)
	v_mfma_f32_32x32x16_bf16 v[108:123], v[200:203], v[48:51], v[108:123]
	s_waitcnt lgkmcnt(4)
	v_mfma_f32_32x32x16_bf16 v[108:123], v[204:207], v[56:59], v[108:123]
	ds_read_b128 v[200:203], v88 offset:32768
	ds_read_b128 v[204:207], v88 offset:33024
	s_waitcnt vmcnt(0)
	s_waitcnt lgkmcnt(2)
	s_barrier
	s_add_u32 s40, s6, 0x18000
	s_addc_u32 s41, s7, 0
	s_mov_b32 s42, m0
	s_mov_b32 m0, s21
	s_nop 0
	global_load_lds_dwordx4 v192, s[40:41]
	s_mov_b32 m0, s42
	s_add_u32 s40, s6, 0x1a000
	s_addc_u32 s41, s7, 0
	s_mov_b32 s42, m0
	s_mov_b32 m0, s31
	s_nop 0
	global_load_lds_dwordx4 v192, s[40:41]
	s_mov_b32 m0, s42
	s_waitcnt lgkmcnt(5)
	v_mfma_f32_32x32x16_bf16 v[108:123], v[92:95], v[36:39], v[108:123]
	s_waitcnt lgkmcnt(4)
	v_mfma_f32_32x32x16_bf16 v[108:123], v[96:99], v[44:47], v[108:123]
	ds_read_b128 v[92:95], v89 offset:32768
	ds_read_b128 v[96:99], v89 offset:33024
	s_add_u32 s40, s6, 0x1c000
	s_addc_u32 s41, s7, 0
	s_mov_b32 s42, m0
	s_mov_b32 m0, s33
	s_nop 0
	global_load_lds_dwordx4 v192, s[40:41]
	s_mov_b32 m0, s42
	s_add_u32 s40, s6, 0x1e000
	s_addc_u32 s41, s7, 0
	s_mov_b32 s42, m0
	s_mov_b32 m0, s34
	s_nop 0
	global_load_lds_dwordx4 v192, s[40:41]
	s_mov_b32 m0, s42
	ds_read_b128 v[128:131], v81
	ds_read_b128 v[132:135], v81 offset:1024
	ds_read_b128 v[136:139], v81 offset:2048
	ds_read_b128 v[140:143], v81 offset:3072
	s_waitcnt lgkmcnt(7)
	v_mfma_f32_32x32x16_bf16 v[108:123], v[200:203], v[28:31], v[108:123]
	s_waitcnt lgkmcnt(6)
	v_mfma_f32_32x32x16_bf16 v[108:123], v[204:207], v[40:43], v[108:123]
	ds_read_b128 v[200:203], v90 offset:32768
	ds_read_b128 v[204:207], v90 offset:33024
	ds_read_b128 v[0:3], v80 offset:512
	ds_read_b128 v[4:7], v80 offset:544
	ds_read_b128 v[8:11], v80 offset:576
	ds_read_b128 v[12:15], v80 offset:608
	s_waitcnt lgkmcnt(11)
	v_mfma_f32_32x32x16_bf16 v[108:123], v[92:95], v[24:27], v[108:123]
	s_waitcnt lgkmcnt(10)
	v_mfma_f32_32x32x16_bf16 v[108:123], v[96:99], v[32:35], v[108:123]
	ds_read_b128 v[92:95], v208
	ds_read_b128 v[96:99], v208 offset:256
	s_waitcnt lgkmcnt(7)
	v_mfma_f32_32x32x16_bf16 v[108:123], v[200:203], v[20:23], v[108:123]
	s_waitcnt lgkmcnt(6)
	v_mfma_f32_32x32x16_bf16 v[108:123], v[204:207], v[16:19], v[108:123]
	ds_read_b128 v[200:203], v209
	ds_read_b128 v[204:207], v209 offset:256
	s_waitcnt lgkmcnt(4)
	s_waitcnt lgkmcnt(3)
	v_mfma_f32_32x32x16_bf16 v[0:15], v[92:95], v[68:71], v[0:15]
	s_waitcnt lgkmcnt(2)
	v_mfma_f32_32x32x16_bf16 v[0:15], v[96:99], v[76:79], v[0:15]
	ds_read_b128 v[92:95], v210
	ds_read_b128 v[96:99], v210 offset:256
	s_waitcnt lgkmcnt(3)
	v_mfma_f32_32x32x16_bf16 v[0:15], v[200:203], v[60:63], v[0:15]
	s_waitcnt lgkmcnt(2)
	v_mfma_f32_32x32x16_bf16 v[0:15], v[204:207], v[72:75], v[0:15]
	ds_read_b128 v[200:203], v211
	ds_read_b128 v[204:207], v211 offset:256
	s_nop 1
	v_cvt_pk_bf16_f32 v216, v108, v109
	v_cvt_pk_bf16_f32 v217, v110, v111
	v_cvt_pk_bf16_f32 v218, v112, v113
	v_cvt_pk_bf16_f32 v219, v114, v115
	s_waitcnt lgkmcnt(3)
	v_mfma_f32_32x32x16_bf16 v[0:15], v[92:95], v[52:55], v[0:15]
	s_waitcnt lgkmcnt(2)
	v_mfma_f32_32x32x16_bf16 v[0:15], v[96:99], v[64:67], v[0:15]
	ds_read_b128 v[92:95], v212
	ds_read_b128 v[96:99], v212 offset:256
	v_cvt_pk_bf16_f32 v220, v116, v117
	v_cvt_pk_bf16_f32 v221, v118, v119
	v_cvt_pk_bf16_f32 v222, v120, v121
	v_cvt_pk_bf16_f32 v223, v122, v123
	ds_write_b128 v82, v[216:219] offset:20480
	ds_write_b128 v82, v[220:223] offset:21504
	s_waitcnt lgkmcnt(5)
	v_mfma_f32_32x32x16_bf16 v[0:15], v[200:203], v[48:51], v[0:15]
	s_waitcnt lgkmcnt(4)
	v_mfma_f32_32x32x16_bf16 v[0:15], v[204:207], v[56:59], v[0:15]
	ds_read_b128 v[200:203], v213
	ds_read_b128 v[204:207], v213 offset:256
	s_waitcnt vmcnt(0)
	s_waitcnt lgkmcnt(2)
	s_barrier
	s_add_u32 s40, s14, 0x0
	s_addc_u32 s41, s15, 0
	s_mov_b32 s42, m0
	s_mov_b32 m0, s23
	s_nop 0
	global_load_lds_dwordx4 v192, s[40:41]
	s_mov_b32 m0, s42
	s_add_u32 s40, s14, 0x2000
	s_addc_u32 s41, s15, 0
	s_mov_b32 s42, m0
	s_mov_b32 m0, s24
	s_nop 0
	global_load_lds_dwordx4 v192, s[40:41]
	s_mov_b32 m0, s42
	s_waitcnt lgkmcnt(5)
	v_mfma_f32_32x32x16_bf16 v[0:15], v[92:95], v[36:39], v[0:15]
	s_waitcnt lgkmcnt(4)
	v_mfma_f32_32x32x16_bf16 v[0:15], v[96:99], v[44:47], v[0:15]
	ds_read_b128 v[92:95], v214
	ds_read_b128 v[96:99], v214 offset:256
	s_add_u32 s40, s14, 0x4000
	s_addc_u32 s41, s15, 0
	s_mov_b32 s42, m0
	s_mov_b32 m0, s25
	s_nop 0
	global_load_lds_dwordx4 v192, s[40:41]
	s_mov_b32 m0, s42
	s_add_u32 s40, s14, 0x6000
	s_addc_u32 s41, s15, 0
	s_mov_b32 s42, m0
	s_mov_b32 m0, s26
	s_nop 0
	global_load_lds_dwordx4 v192, s[40:41]
	s_mov_b32 m0, s42
	ds_read_b128 v[144:147], v81 offset:20480
	ds_read_b128 v[148:151], v81 offset:21504
	ds_read_b128 v[152:155], v81 offset:22528
	ds_read_b128 v[156:159], v81 offset:23552
	s_waitcnt lgkmcnt(7)
	v_mfma_f32_32x32x16_bf16 v[0:15], v[200:203], v[28:31], v[0:15]
	s_waitcnt lgkmcnt(6)
	v_mfma_f32_32x32x16_bf16 v[0:15], v[204:207], v[40:43], v[0:15]
	ds_read_b128 v[200:203], v215
	ds_read_b128 v[204:207], v215 offset:256
	ds_read_b128 v[108:111], v80 offset:768
	ds_read_b128 v[112:115], v80 offset:800
	ds_read_b128 v[116:119], v80 offset:832
	ds_read_b128 v[120:123], v80 offset:864
	s_waitcnt lgkmcnt(11)
	v_mfma_f32_32x32x16_bf16 v[0:15], v[92:95], v[24:27], v[0:15]
	s_waitcnt lgkmcnt(10)
	v_mfma_f32_32x32x16_bf16 v[0:15], v[96:99], v[32:35], v[0:15]
	ds_read_b128 v[92:95], v83
	ds_read_b128 v[96:99], v83 offset:256
	s_waitcnt lgkmcnt(7)
	v_mfma_f32_32x32x16_bf16 v[0:15], v[200:203], v[20:23], v[0:15]
	s_waitcnt lgkmcnt(6)
	v_mfma_f32_32x32x16_bf16 v[0:15], v[204:207], v[16:19], v[0:15]
	ds_read_b128 v[200:203], v84
	ds_read_b128 v[204:207], v84 offset:256
	s_waitcnt lgkmcnt(4)
	s_waitcnt lgkmcnt(3)
	v_mfma_f32_32x32x16_bf16 v[108:123], v[92:95], v[68:71], v[108:123]
	s_waitcnt lgkmcnt(2)
	v_mfma_f32_32x32x16_bf16 v[108:123], v[96:99], v[76:79], v[108:123]
	ds_read_b128 v[92:95], v85
	ds_read_b128 v[96:99], v85 offset:256
	s_waitcnt lgkmcnt(3)
	v_mfma_f32_32x32x16_bf16 v[108:123], v[200:203], v[60:63], v[108:123]
	s_waitcnt lgkmcnt(2)
	v_mfma_f32_32x32x16_bf16 v[108:123], v[204:207], v[72:75], v[108:123]
	ds_read_b128 v[200:203], v86
	ds_read_b128 v[204:207], v86 offset:256
	s_nop 1
	v_cvt_pk_bf16_f32 v216, v0, v1
	v_cvt_pk_bf16_f32 v217, v2, v3
	v_cvt_pk_bf16_f32 v218, v4, v5
	v_cvt_pk_bf16_f32 v219, v6, v7
	s_waitcnt lgkmcnt(3)
	v_mfma_f32_32x32x16_bf16 v[108:123], v[92:95], v[52:55], v[108:123]
	s_waitcnt lgkmcnt(2)
	v_mfma_f32_32x32x16_bf16 v[108:123], v[96:99], v[64:67], v[108:123]
	ds_read_b128 v[92:95], v87
	ds_read_b128 v[96:99], v87 offset:256
	v_cvt_pk_bf16_f32 v220, v8, v9
	v_cvt_pk_bf16_f32 v221, v10, v11
	v_cvt_pk_bf16_f32 v222, v12, v13
	v_cvt_pk_bf16_f32 v223, v14, v15
	ds_write_b128 v82, v[216:219]
	ds_write_b128 v82, v[220:223] offset:1024
	s_waitcnt lgkmcnt(5)
	v_mfma_f32_32x32x16_bf16 v[108:123], v[200:203], v[48:51], v[108:123]
	s_waitcnt lgkmcnt(4)
	v_mfma_f32_32x32x16_bf16 v[108:123], v[204:207], v[56:59], v[108:123]
	ds_read_b128 v[200:203], v88
	ds_read_b128 v[204:207], v88 offset:256
	s_waitcnt lgkmcnt(2)
	s_barrier
	s_add_u32 s40, s14, 0x8000
	s_addc_u32 s41, s15, 0
	s_mov_b32 s42, m0
	s_mov_b32 m0, s27
	s_nop 0
	global_load_lds_dwordx4 v192, s[40:41]
	s_mov_b32 m0, s42
	s_add_u32 s40, s14, 0xa000
	s_addc_u32 s41, s15, 0
	s_mov_b32 s42, m0
	s_mov_b32 m0, s28
	s_nop 0
	global_load_lds_dwordx4 v192, s[40:41]
	s_mov_b32 m0, s42
	s_waitcnt lgkmcnt(5)
	v_mfma_f32_32x32x16_bf16 v[108:123], v[92:95], v[36:39], v[108:123]
	s_waitcnt lgkmcnt(4)
	v_mfma_f32_32x32x16_bf16 v[108:123], v[96:99], v[44:47], v[108:123]
	ds_read_b128 v[92:95], v89
	ds_read_b128 v[96:99], v89 offset:256
	s_add_u32 s40, s14, 0xc000
	s_addc_u32 s41, s15, 0
	s_mov_b32 s42, m0
	s_mov_b32 m0, s29
	s_nop 0
	global_load_lds_dwordx4 v192, s[40:41]
	s_mov_b32 m0, s42
	s_add_u32 s40, s14, 0xe000
	s_addc_u32 s41, s15, 0
	s_mov_b32 s42, m0
	s_mov_b32 m0, s30
	s_nop 0
	global_load_lds_dwordx4 v192, s[40:41]
	s_mov_b32 m0, s42
	ds_read_b128 v[160:163], v81
	ds_read_b128 v[164:167], v81 offset:1024
	ds_read_b128 v[168:171], v81 offset:2048
	ds_read_b128 v[172:175], v81 offset:3072
	s_waitcnt lgkmcnt(7)
	v_mfma_f32_32x32x16_bf16 v[108:123], v[200:203], v[28:31], v[108:123]
	s_waitcnt lgkmcnt(6)
	v_mfma_f32_32x32x16_bf16 v[108:123], v[204:207], v[40:43], v[108:123]
	ds_read_b128 v[200:203], v90
	ds_read_b128 v[204:207], v90 offset:256
	s_waitcnt lgkmcnt(7)
	v_mfma_f32_32x32x16_bf16 v[108:123], v[92:95], v[24:27], v[108:123]
	s_waitcnt lgkmcnt(6)
	v_mfma_f32_32x32x16_bf16 v[108:123], v[96:99], v[32:35], v[108:123]
	s_waitcnt lgkmcnt(1)
	v_mfma_f32_32x32x16_bf16 v[108:123], v[200:203], v[20:23], v[108:123]
	s_waitcnt lgkmcnt(0)
	v_mfma_f32_32x32x16_bf16 v[108:123], v[204:207], v[16:19], v[108:123]
	s_nop 11
	s_nop 2
	v_cvt_pk_bf16_f32 v216, v108, v109
	v_cvt_pk_bf16_f32 v217, v110, v111
	v_cvt_pk_bf16_f32 v218, v112, v113
	v_cvt_pk_bf16_f32 v219, v114, v115
	v_cvt_pk_bf16_f32 v220, v116, v117
	v_cvt_pk_bf16_f32 v221, v118, v119
	v_cvt_pk_bf16_f32 v222, v120, v121
	v_cvt_pk_bf16_f32 v223, v122, v123
	ds_write_b128 v82, v[216:219] offset:20480
	ds_write_b128 v82, v[220:223] offset:21504
	v_mbcnt_lo_u32_b32 v224, -1, 0
	v_mbcnt_hi_u32_b32 v193, -1, v224
	v_mov_b32_e32 v194, v193
	s_waitcnt vmcnt(4) lgkmcnt(0)
	s_barrier
	ds_read_b128 v[176:179], v81 offset:20480
	ds_read_b128 v[180:183], v81 offset:21504
	ds_read_b128 v[184:187], v81 offset:22528
	ds_read_b128 v[188:191], v81 offset:23552
	s_movk_i32 s7, 0x80
	s_movk_i32 s6, 0xc0
	s_mov_b32 s5, 0x10000
	s_waitcnt lgkmcnt(0)
	s_barrier
	s_cmpk_gt_u32 s3, 0xff
	s_nop 0
	v_and_b32_e32 v196, 31, v194
	v_ashrrev_i32_e32 v197, 5, v194
	v_lshlrev_b32_e32 v195, 2, v194
	v_bfe_u32 v198, v194, 2, 2
	s_cbranch_scc0 .LBB1_16
	v_lshl_add_u32 v0, s20, 2, v197
	v_lshlrev_b32_e32 v3, 2, v197
	v_add_u32_e32 v1, 2, v0
	v_lshlrev_b32_e32 v2, 9, v0
	v_and_b32_e32 v3, 12, v3
	v_bfe_u32 v0, v0, 2, 2
	v_bitop3_b32 v0, v0, v196, v3 bitop3:0x36
	v_lshl_or_b32 v199, v0, 4, v2
	v_lshlrev_b32_e32 v0, 2, v1
	s_bfe_u32 s18, s3, 0x10006
	v_and_b32_e32 v0, 12, v0
	v_bfe_u32 v2, v1, 2, 2
	v_bitop3_b32 v0, v0, v196, v2 bitop3:0x36
	v_lshrrev_b32_e32 v2, 3, v194
	s_lshl_b32 s16, s18, 8
	v_and_b32_e32 v2, 2, v2
	v_bfe_u32 v3, v194, 1, 1
	s_add_i32 s16, s16, 0
	v_lshlrev_b32_e32 v4, 3, v194
	v_lshl_add_u32 v5, v197, 11, s16
	v_bitop3_b32 v2, v2, v197, v3 bitop3:0x36
	v_and_or_b32 v4, v4, 8, v5
	v_lshlrev_b32_e32 v2, 4, v2
	v_lshlrev_b32_e32 v3, 6, v198
	v_lshl_add_u32 v4, v198, 9, v4
	v_or_b32_e32 v5, v2, v3
	v_add_u32_e32 v200, v4, v5
	v_bitop3_b32 v5, v2, v3, 32 bitop3:0xde
	v_add_u32_e32 v6, 0x1000, v4
	v_add_u32_e32 v201, v6, v5
	v_xor_b32_e32 v5, 64, v3
	v_bitop3_b32 v5, v2, v5, 32 bitop3:0xde
	v_add_u32_e32 v203, v6, v5
	v_xor_b32_e32 v5, 0x80, v3
	v_bitop3_b32 v7, v2, v3, 64 bitop3:0xf6
	v_bitop3_b32 v5, v2, v5, 32 bitop3:0xde
	v_add_u32_e32 v202, v4, v7
	v_bitop3_b32 v7, v2, v3, s7 bitop3:0xf6
	v_add_u32_e32 v205, v6, v5
	v_xor_b32_e32 v5, 0xc0, v3
	v_bitop3_b32 v3, v2, v3, s6 bitop3:0xf6
	s_and_b32 s6, s22, 2
	v_lshlrev_b32_e32 v1, 9, v1
	s_lshl_b32 s27, s6, 2
	s_lshl_b32 s7, s6, 8
	s_lshl_b32 s6, s6, 12
	v_lshl_or_b32 v208, v0, 4, v1
	s_lshl_b32 s19, s20, 11
	s_add_i32 s7, s7, 0
	s_add_i32 s6, s6, 0
	v_mov_b32_e32 v0, 0
	v_bitop3_b32 v2, v2, v5, 32 bitop3:0xde
	s_waitcnt vmcnt(0)
	s_add_i32 s19, s19, 0
	s_add_i32 s16, s7, 0x20000
	s_add_i32 s7, s7, 0x20100
	v_lshlrev_b32_e32 v209, 4, v194
	s_add_i32 s6, s6, 0x18000
	v_mov_b32_e32 v14, v0
	v_mov_b32_e32 v15, v0
	v_add_u32_e32 v204, v4, v7
	v_add_u32_e32 v206, v4, v3
	v_add_u32_e32 v207, v6, v2
	v_add_u32_e32 v212, s6, v209
	s_add_u32 s6, s8, 0xfff90000
	v_mov_b32_e32 v1, v0
	v_mov_b32_e32 v2, v0
	v_mov_b32_e32 v3, v0
	v_mov_b32_e32 v4, v0
	v_mov_b32_e32 v5, v0
	v_mov_b32_e32 v6, v0
	v_mov_b32_e32 v7, v0
	v_mov_b32_e32 v8, v0
	v_mov_b32_e32 v9, v0
	v_mov_b32_e32 v10, v0
	v_mov_b32_e32 v11, v0
	v_mov_b32_e32 v12, v0
	v_mov_b32_e32 v13, v0
	v_mov_b64_e32 v[62:63], v[14:15]
	v_mov_b64_e32 v[94:95], v[14:15]
	v_mov_b64_e32 v[126:127], v[14:15]
	v_mov_b64_e32 v[30:31], v[14:15]
	v_mov_b64_e32 v[46:47], v[14:15]
	v_mov_b64_e32 v[78:79], v[14:15]
	v_mov_b64_e32 v[110:111], v[14:15]
	v_add_u32_e32 v210, s16, v195
	v_add_u32_e32 v211, s7, v195
	s_addc_u32 s7, s9, -1
	s_mov_b32 s33, 1
	s_mov_b32 s31, 0x8000
	s_mov_b32 s29, 0x10000
	v_mov_b64_e32 v[60:61], v[12:13]
	v_mov_b64_e32 v[58:59], v[10:11]
	v_mov_b64_e32 v[56:57], v[8:9]
	v_mov_b64_e32 v[54:55], v[6:7]
	v_mov_b64_e32 v[52:53], v[4:5]
	v_mov_b64_e32 v[50:51], v[2:3]
	v_mov_b64_e32 v[48:49], v[0:1]
	v_mov_b64_e32 v[92:93], v[12:13]
	v_mov_b64_e32 v[90:91], v[10:11]
	v_mov_b64_e32 v[88:89], v[8:9]
	v_mov_b64_e32 v[86:87], v[6:7]
	v_mov_b64_e32 v[84:85], v[4:5]
	v_mov_b64_e32 v[82:83], v[2:3]
	v_mov_b64_e32 v[80:81], v[0:1]
	v_mov_b64_e32 v[124:125], v[12:13]
	v_mov_b64_e32 v[122:123], v[10:11]
	v_mov_b64_e32 v[120:121], v[8:9]
	v_mov_b64_e32 v[118:119], v[6:7]
	v_mov_b64_e32 v[116:117], v[4:5]
	v_mov_b64_e32 v[114:115], v[2:3]
	v_mov_b64_e32 v[112:113], v[0:1]
	v_mov_b64_e32 v[28:29], v[12:13]
	v_mov_b64_e32 v[26:27], v[10:11]
	v_mov_b64_e32 v[24:25], v[8:9]
	v_mov_b64_e32 v[22:23], v[6:7]
	v_mov_b64_e32 v[20:21], v[4:5]
	v_mov_b64_e32 v[18:19], v[2:3]
	v_mov_b64_e32 v[16:17], v[0:1]
	v_mov_b64_e32 v[44:45], v[12:13]
	v_mov_b64_e32 v[42:43], v[10:11]
	v_mov_b64_e32 v[40:41], v[8:9]
	v_mov_b64_e32 v[38:39], v[6:7]
	v_mov_b64_e32 v[36:37], v[4:5]
	v_mov_b64_e32 v[34:35], v[2:3]
	v_mov_b64_e32 v[32:33], v[0:1]
	v_mov_b64_e32 v[76:77], v[12:13]
	v_mov_b64_e32 v[74:75], v[10:11]
	v_mov_b64_e32 v[72:73], v[8:9]
	v_mov_b64_e32 v[70:71], v[6:7]
	v_mov_b64_e32 v[68:69], v[4:5]
	v_mov_b64_e32 v[66:67], v[2:3]
	v_mov_b64_e32 v[64:65], v[0:1]
	v_mov_b64_e32 v[108:109], v[12:13]
	v_mov_b64_e32 v[106:107], v[10:11]
	v_mov_b64_e32 v[104:105], v[8:9]
	v_mov_b64_e32 v[102:103], v[6:7]
	v_mov_b64_e32 v[100:101], v[4:5]
	v_mov_b64_e32 v[98:99], v[2:3]
	v_mov_b64_e32 v[96:97], v[0:1]
	s_waitcnt lgkmcnt(0)
	s_barrier
